# refine unit: five K/V register buffers (four groups ahead), 256 VGPRs
# speedup vs baseline: 1.0049x; 1.0049x over previous
.LBB2_14:
	s_and_b32 s28, s34, 15
	s_ff1_i32_b64 s37, s[30:31]
	s_lshl_b32 s28, s28, 7
	v_lshl_add_u64 v[14:15], v[4:5], 0, s[28:29]
	v_lshl_add_u64 v[16:17], v[6:7], 0, s[28:29]
	v_lshl_add_u64 v[18:19], v[8:9], 0, s[28:29]
	v_lshl_add_u64 v[20:21], v[10:11], 0, s[28:29]
	s_add_i32 s28, s39, s37
	s_lshl_b32 s30, s34, 1
	v_lshl_or_b32 v22, s28, 6, v2
	v_and_or_b32 v22, s30, 32, v22
	v_mov_b32_e32 v23, v1
	v_lshlrev_b64 v[24:25], 12, v[22:23]
	s_and_b32 s36, s34, 31
	v_lshl_add_u64 v[22:23], s[12:13], 0, v[24:25]
	v_lshl_add_u64 v[24:25], s[14:15], 0, v[24:25]
	v_accvgpr_write_b32 a15, 0
	v_accvgpr_write_b32 a14, 0
	v_accvgpr_write_b32 a13, 0
	v_accvgpr_write_b32 a12, 0
	v_accvgpr_write_b32 a11, 0
	v_accvgpr_write_b32 a10, 0
	v_accvgpr_write_b32 a9, 0
	v_accvgpr_write_b32 a8, 0
	v_accvgpr_write_b32 a7, 0
	v_accvgpr_write_b32 a6, 0
	v_accvgpr_write_b32 a5, 0
	v_accvgpr_write_b32 a4, 0
	v_accvgpr_write_b32 a3, 0
	v_accvgpr_write_b32 a2, 0
	v_accvgpr_write_b32 a1, 0
	v_accvgpr_write_b32 a0, 0
	s_mov_b64 s[30:31], 0
	v_lshl_add_u64 v[214:215], v[22:23], 0, v[12:13]
	v_lshl_add_u64 v[216:217], v[24:25], 0, v[12:13]
	v_readfirstlane_b32 s30, v16
	v_readfirstlane_b32 s31, v17
	v_readfirstlane_b32 s41, v0
	v_lshrrev_b32_e32 v223, 3, v26
	v_and_b32_e32 v218, 7, v26
	v_lshlrev_b32_e32 v223, 11, v223
	v_lshl_or_b32 v218, v218, 4, v223
	v_mov_b32_e32 v219, 0
	v_lshl_add_u64 v[220:221], v[218:219], 0, s[30:31]
	s_lshr_b32 s41, s41, 6
	s_mul_i32 s40, s41, 12288
	s_add_i32 s40, s40, 16448
	s_mov_b32 s43, 0
	v_lshrrev_b32_e32 v223, 5, v26
	v_and_b32_e32 v222, 31, v26
	v_lshlrev_b32_e32 v223, 9, v223
	v_lshl_or_b32 v222, v222, 2, v223
	v_add_u32_e32 v222, s40, v222
	s_add_i32 s28, s40, 0
	s_mov_b32 s42, 0x0
	s_mov_b32 m0, s28
	v_lshl_add_u64 v[218:219], v[220:221], 0, s[42:43]
	global_load_lds_dwordx4 v[218:219], off
	s_add_i32 s28, s40, 1024
	s_mov_b32 s42, 0x4000
	s_mov_b32 m0, s28
	v_lshl_add_u64 v[218:219], v[220:221], 0, s[42:43]
	global_load_lds_dwordx4 v[218:219], off
	s_add_i32 s28, s40, 2048
	s_mov_b32 s42, 0x8000
	s_mov_b32 m0, s28
	v_lshl_add_u64 v[218:219], v[220:221], 0, s[42:43]
	global_load_lds_dwordx4 v[218:219], off
	s_add_i32 s28, s40, 3072
	s_mov_b32 s42, 0xc000
	s_mov_b32 m0, s28
	v_lshl_add_u64 v[218:219], v[220:221], 0, s[42:43]
	global_load_lds_dwordx4 v[218:219], off
	global_load_dwordx4 v[38:41], v[214:215], off offset:0
	global_load_dwordx4 v[54:57], v[216:217], off offset:0
	global_load_dwordx4 v[42:45], v[214:215], off offset:32
	global_load_dwordx4 v[58:61], v[216:217], off offset:32
	global_load_dwordx4 v[46:49], v[214:215], off offset:64
	global_load_dwordx4 v[62:65], v[216:217], off offset:64
	global_load_dwordx4 v[50:53], v[214:215], off offset:96
	global_load_dwordx4 v[66:69], v[216:217], off offset:96
	s_add_i32 s28, s40, 4096
	s_mov_b32 s42, 0x10000
	s_mov_b32 m0, s28
	v_lshl_add_u64 v[218:219], v[220:221], 0, s[42:43]
	global_load_lds_dwordx4 v[218:219], off
	s_add_i32 s28, s40, 5120
	s_mov_b32 s42, 0x14000
	s_mov_b32 m0, s28
	v_lshl_add_u64 v[218:219], v[220:221], 0, s[42:43]
	global_load_lds_dwordx4 v[218:219], off
	s_add_i32 s28, s40, 6144
	s_mov_b32 s42, 0x18000
	s_mov_b32 m0, s28
	v_lshl_add_u64 v[218:219], v[220:221], 0, s[42:43]
	global_load_lds_dwordx4 v[218:219], off
	s_add_i32 s28, s40, 7168
	s_mov_b32 s42, 0x1c000
	s_mov_b32 m0, s28
	v_lshl_add_u64 v[218:219], v[220:221], 0, s[42:43]
	global_load_lds_dwordx4 v[218:219], off
	global_load_dwordx4 v[70:73], v[214:215], off offset:128
	global_load_dwordx4 v[86:89], v[216:217], off offset:128
	global_load_dwordx4 v[74:77], v[214:215], off offset:160
	global_load_dwordx4 v[90:93], v[216:217], off offset:160
	global_load_dwordx4 v[78:81], v[214:215], off offset:192
	global_load_dwordx4 v[94:97], v[216:217], off offset:192
	global_load_dwordx4 v[82:85], v[214:215], off offset:224
	global_load_dwordx4 v[98:101], v[216:217], off offset:224
	global_load_dwordx4 v[102:105], v[214:215], off offset:256
	global_load_dwordx4 v[118:121], v[216:217], off offset:256
	global_load_dwordx4 v[106:109], v[214:215], off offset:288
	global_load_dwordx4 v[122:125], v[216:217], off offset:288
	global_load_dwordx4 v[110:113], v[214:215], off offset:320
	global_load_dwordx4 v[126:129], v[216:217], off offset:320
	global_load_dwordx4 v[114:117], v[214:215], off offset:352
	global_load_dwordx4 v[130:133], v[216:217], off offset:352
	global_load_dwordx4 v[134:137], v[214:215], off offset:384
	global_load_dwordx4 v[150:153], v[216:217], off offset:384
	global_load_dwordx4 v[138:141], v[214:215], off offset:416
	global_load_dwordx4 v[154:157], v[216:217], off offset:416
	global_load_dwordx4 v[142:145], v[214:215], off offset:448
	global_load_dwordx4 v[158:161], v[216:217], off offset:448
	global_load_dwordx4 v[146:149], v[214:215], off offset:480
	global_load_dwordx4 v[162:165], v[216:217], off offset:480
	s_waitcnt vmcnt(36)
	s_waitcnt vmcnt(28)
	ds_read_b32 v198, v222 offset:0
	ds_read_b32 v199, v222 offset:128
	ds_read_b32 v200, v222 offset:256
	ds_read_b32 v201, v222 offset:384
	ds_read_b32 v202, v222 offset:1024
	ds_read_b32 v203, v222 offset:1152
	ds_read_b32 v204, v222 offset:1280
	ds_read_b32 v205, v222 offset:1408
	ds_read_b32 v206, v222 offset:2048
	ds_read_b32 v207, v222 offset:2176
	ds_read_b32 v208, v222 offset:2304
	ds_read_b32 v209, v222 offset:2432
	ds_read_b32 v210, v222 offset:3072
	ds_read_b32 v211, v222 offset:3200
	ds_read_b32 v212, v222 offset:3328
	ds_read_b32 v213, v222 offset:3456
	s_add_i32 s28, s40, 8192
	s_mov_b32 s42, 0x20000
	s_mov_b32 m0, s28
	v_lshl_add_u64 v[218:219], v[220:221], 0, s[42:43]
	global_load_lds_dwordx4 v[218:219], off
	s_add_i32 s28, s40, 9216
	s_mov_b32 s42, 0x24000
	s_mov_b32 m0, s28
	v_lshl_add_u64 v[218:219], v[220:221], 0, s[42:43]
	global_load_lds_dwordx4 v[218:219], off
	s_add_i32 s28, s40, 10240
	s_mov_b32 s42, 0x28000
	s_mov_b32 m0, s28
	v_lshl_add_u64 v[218:219], v[220:221], 0, s[42:43]
	global_load_lds_dwordx4 v[218:219], off
	s_add_i32 s28, s40, 11264
	s_mov_b32 s42, 0x2c000
	s_mov_b32 m0, s28
	v_lshl_add_u64 v[218:219], v[220:221], 0, s[42:43]
	global_load_lds_dwordx4 v[218:219], off
	global_load_dwordx4 v[166:169], v[214:215], off offset:512
	global_load_dwordx4 v[182:185], v[216:217], off offset:512
	global_load_dwordx4 v[170:173], v[214:215], off offset:544
	global_load_dwordx4 v[186:189], v[216:217], off offset:544
	global_load_dwordx4 v[174:177], v[214:215], off offset:576
	global_load_dwordx4 v[190:193], v[216:217], off offset:576
	global_load_dwordx4 v[178:181], v[214:215], off offset:608
	global_load_dwordx4 v[194:197], v[216:217], off offset:608
	v_add_f32_e32 v38, v38, v54
	v_mul_f32_e32 v38, 0.5, v38
	v_add_f32_e32 v39, v39, v55
	v_mul_f32_e32 v39, 0.5, v39
	v_add_f32_e32 v40, v40, v56
	v_mul_f32_e32 v40, 0.5, v40
	s_waitcnt lgkmcnt(15)
	v_mfma_f32_32x32x2_f32 a[0:15], v38, v198, a[0:15]
	v_add_f32_e32 v41, v41, v57
	v_mul_f32_e32 v41, 0.5, v41
	s_waitcnt lgkmcnt(14)
	v_mfma_f32_32x32x2_f32 a[0:15], v39, v199, a[0:15]
	v_add_f32_e32 v42, v42, v58
	v_mul_f32_e32 v42, 0.5, v42
	s_waitcnt lgkmcnt(13)
	v_mfma_f32_32x32x2_f32 a[0:15], v40, v200, a[0:15]
	v_add_f32_e32 v43, v43, v59
	v_mul_f32_e32 v43, 0.5, v43
	s_waitcnt lgkmcnt(12)
	v_mfma_f32_32x32x2_f32 a[0:15], v41, v201, a[0:15]
	v_add_f32_e32 v44, v44, v60
	v_mul_f32_e32 v44, 0.5, v44
	s_waitcnt lgkmcnt(11)
	v_mfma_f32_32x32x2_f32 a[0:15], v42, v202, a[0:15]
	v_add_f32_e32 v45, v45, v61
	v_mul_f32_e32 v45, 0.5, v45
	s_waitcnt lgkmcnt(10)
	v_mfma_f32_32x32x2_f32 a[0:15], v43, v203, a[0:15]
	v_add_f32_e32 v46, v46, v62
	v_mul_f32_e32 v46, 0.5, v46
	s_waitcnt lgkmcnt(9)
	v_mfma_f32_32x32x2_f32 a[0:15], v44, v204, a[0:15]
	v_add_f32_e32 v47, v47, v63
	v_mul_f32_e32 v47, 0.5, v47
	s_waitcnt lgkmcnt(8)
	v_mfma_f32_32x32x2_f32 a[0:15], v45, v205, a[0:15]
	v_add_f32_e32 v48, v48, v64
	v_mul_f32_e32 v48, 0.5, v48
	s_waitcnt lgkmcnt(7)
	v_mfma_f32_32x32x2_f32 a[0:15], v46, v206, a[0:15]
	v_add_f32_e32 v49, v49, v65
	v_mul_f32_e32 v49, 0.5, v49
	s_waitcnt lgkmcnt(6)
	v_mfma_f32_32x32x2_f32 a[0:15], v47, v207, a[0:15]
	v_add_f32_e32 v50, v50, v66
	v_mul_f32_e32 v50, 0.5, v50
	s_waitcnt lgkmcnt(5)
	v_mfma_f32_32x32x2_f32 a[0:15], v48, v208, a[0:15]
	v_add_f32_e32 v51, v51, v67
	v_mul_f32_e32 v51, 0.5, v51
	s_waitcnt lgkmcnt(4)
	v_mfma_f32_32x32x2_f32 a[0:15], v49, v209, a[0:15]
	v_add_f32_e32 v52, v52, v68
	v_mul_f32_e32 v52, 0.5, v52
	s_waitcnt lgkmcnt(3)
	v_mfma_f32_32x32x2_f32 a[0:15], v50, v210, a[0:15]
	v_add_f32_e32 v53, v53, v69
	v_mul_f32_e32 v53, 0.5, v53
	s_waitcnt lgkmcnt(2)
	v_mfma_f32_32x32x2_f32 a[0:15], v51, v211, a[0:15]
	s_waitcnt lgkmcnt(1)
	v_mfma_f32_32x32x2_f32 a[0:15], v52, v212, a[0:15]
	s_waitcnt lgkmcnt(0)
	v_mfma_f32_32x32x2_f32 a[0:15], v53, v213, a[0:15]
	s_waitcnt vmcnt(36)
	s_waitcnt vmcnt(28)
	ds_read_b32 v198, v222 offset:4096
	ds_read_b32 v199, v222 offset:4224
	ds_read_b32 v200, v222 offset:4352
	ds_read_b32 v201, v222 offset:4480
	ds_read_b32 v202, v222 offset:5120
	ds_read_b32 v203, v222 offset:5248
	ds_read_b32 v204, v222 offset:5376
	ds_read_b32 v205, v222 offset:5504
	ds_read_b32 v206, v222 offset:6144
	ds_read_b32 v207, v222 offset:6272
	ds_read_b32 v208, v222 offset:6400
	ds_read_b32 v209, v222 offset:6528
	ds_read_b32 v210, v222 offset:7168
	ds_read_b32 v211, v222 offset:7296
	ds_read_b32 v212, v222 offset:7424
	ds_read_b32 v213, v222 offset:7552
	s_add_i32 s28, s40, 0
	s_mov_b32 s42, 0x30000
	s_mov_b32 m0, s28
	v_lshl_add_u64 v[218:219], v[220:221], 0, s[42:43]
	global_load_lds_dwordx4 v[218:219], off
	s_add_i32 s28, s40, 1024
	s_mov_b32 s42, 0x34000
	s_mov_b32 m0, s28
	v_lshl_add_u64 v[218:219], v[220:221], 0, s[42:43]
	global_load_lds_dwordx4 v[218:219], off
	s_add_i32 s28, s40, 2048
	s_mov_b32 s42, 0x38000
	s_mov_b32 m0, s28
	v_lshl_add_u64 v[218:219], v[220:221], 0, s[42:43]
	global_load_lds_dwordx4 v[218:219], off
	s_add_i32 s28, s40, 3072
	s_mov_b32 s42, 0x3c000
	s_mov_b32 m0, s28
	v_lshl_add_u64 v[218:219], v[220:221], 0, s[42:43]
	global_load_lds_dwordx4 v[218:219], off
	global_load_dwordx4 v[38:41], v[214:215], off offset:640
	global_load_dwordx4 v[54:57], v[216:217], off offset:640
	global_load_dwordx4 v[42:45], v[214:215], off offset:672
	global_load_dwordx4 v[58:61], v[216:217], off offset:672
	global_load_dwordx4 v[46:49], v[214:215], off offset:704
	global_load_dwordx4 v[62:65], v[216:217], off offset:704
	global_load_dwordx4 v[50:53], v[214:215], off offset:736
	global_load_dwordx4 v[66:69], v[216:217], off offset:736
	v_add_f32_e32 v70, v70, v86
	v_mul_f32_e32 v70, 0.5, v70
	v_add_f32_e32 v71, v71, v87
	v_mul_f32_e32 v71, 0.5, v71
	v_add_f32_e32 v72, v72, v88
	v_mul_f32_e32 v72, 0.5, v72
	s_waitcnt lgkmcnt(15)
	v_mfma_f32_32x32x2_f32 a[0:15], v70, v198, a[0:15]
	v_add_f32_e32 v73, v73, v89
	v_mul_f32_e32 v73, 0.5, v73
	s_waitcnt lgkmcnt(14)
	v_mfma_f32_32x32x2_f32 a[0:15], v71, v199, a[0:15]
	v_add_f32_e32 v74, v74, v90
	v_mul_f32_e32 v74, 0.5, v74
	s_waitcnt lgkmcnt(13)
	v_mfma_f32_32x32x2_f32 a[0:15], v72, v200, a[0:15]
	v_add_f32_e32 v75, v75, v91
	v_mul_f32_e32 v75, 0.5, v75
	s_waitcnt lgkmcnt(12)
	v_mfma_f32_32x32x2_f32 a[0:15], v73, v201, a[0:15]
	v_add_f32_e32 v76, v76, v92
	v_mul_f32_e32 v76, 0.5, v76
	s_waitcnt lgkmcnt(11)
	v_mfma_f32_32x32x2_f32 a[0:15], v74, v202, a[0:15]
	v_add_f32_e32 v77, v77, v93
	v_mul_f32_e32 v77, 0.5, v77
	s_waitcnt lgkmcnt(10)
	v_mfma_f32_32x32x2_f32 a[0:15], v75, v203, a[0:15]
	v_add_f32_e32 v78, v78, v94
	v_mul_f32_e32 v78, 0.5, v78
	s_waitcnt lgkmcnt(9)
	v_mfma_f32_32x32x2_f32 a[0:15], v76, v204, a[0:15]
	v_add_f32_e32 v79, v79, v95
	v_mul_f32_e32 v79, 0.5, v79
	s_waitcnt lgkmcnt(8)
	v_mfma_f32_32x32x2_f32 a[0:15], v77, v205, a[0:15]
	v_add_f32_e32 v80, v80, v96
	v_mul_f32_e32 v80, 0.5, v80
	s_waitcnt lgkmcnt(7)
	v_mfma_f32_32x32x2_f32 a[0:15], v78, v206, a[0:15]
	v_add_f32_e32 v81, v81, v97
	v_mul_f32_e32 v81, 0.5, v81
	s_waitcnt lgkmcnt(6)
	v_mfma_f32_32x32x2_f32 a[0:15], v79, v207, a[0:15]
	v_add_f32_e32 v82, v82, v98
	v_mul_f32_e32 v82, 0.5, v82
	s_waitcnt lgkmcnt(5)
	v_mfma_f32_32x32x2_f32 a[0:15], v80, v208, a[0:15]
	v_add_f32_e32 v83, v83, v99
	v_mul_f32_e32 v83, 0.5, v83
	s_waitcnt lgkmcnt(4)
	v_mfma_f32_32x32x2_f32 a[0:15], v81, v209, a[0:15]
	v_add_f32_e32 v84, v84, v100
	v_mul_f32_e32 v84, 0.5, v84
	s_waitcnt lgkmcnt(3)
	v_mfma_f32_32x32x2_f32 a[0:15], v82, v210, a[0:15]
	v_add_f32_e32 v85, v85, v101
	v_mul_f32_e32 v85, 0.5, v85
	s_waitcnt lgkmcnt(2)
	v_mfma_f32_32x32x2_f32 a[0:15], v83, v211, a[0:15]
	s_waitcnt lgkmcnt(1)
	v_mfma_f32_32x32x2_f32 a[0:15], v84, v212, a[0:15]
	s_waitcnt lgkmcnt(0)
	v_mfma_f32_32x32x2_f32 a[0:15], v85, v213, a[0:15]
	s_waitcnt vmcnt(20)
	ds_read_b32 v198, v222 offset:8192
	ds_read_b32 v199, v222 offset:8320
	ds_read_b32 v200, v222 offset:8448
	ds_read_b32 v201, v222 offset:8576
	ds_read_b32 v202, v222 offset:9216
	ds_read_b32 v203, v222 offset:9344
	ds_read_b32 v204, v222 offset:9472
	ds_read_b32 v205, v222 offset:9600
	ds_read_b32 v206, v222 offset:10240
	ds_read_b32 v207, v222 offset:10368
	ds_read_b32 v208, v222 offset:10496
	ds_read_b32 v209, v222 offset:10624
	ds_read_b32 v210, v222 offset:11264
	ds_read_b32 v211, v222 offset:11392
	ds_read_b32 v212, v222 offset:11520
	ds_read_b32 v213, v222 offset:11648
	s_add_i32 s28, s40, 4096
	s_mov_b32 s42, 0x40000
	s_mov_b32 m0, s28
	v_lshl_add_u64 v[218:219], v[220:221], 0, s[42:43]
	global_load_lds_dwordx4 v[218:219], off
	s_add_i32 s28, s40, 5120
	s_mov_b32 s42, 0x44000
	s_mov_b32 m0, s28
	v_lshl_add_u64 v[218:219], v[220:221], 0, s[42:43]
	global_load_lds_dwordx4 v[218:219], off
	s_add_i32 s28, s40, 6144
	s_mov_b32 s42, 0x48000
	s_mov_b32 m0, s28
	v_lshl_add_u64 v[218:219], v[220:221], 0, s[42:43]
	global_load_lds_dwordx4 v[218:219], off
	s_add_i32 s28, s40, 7168
	s_mov_b32 s42, 0x4c000
	s_mov_b32 m0, s28
	v_lshl_add_u64 v[218:219], v[220:221], 0, s[42:43]
	global_load_lds_dwordx4 v[218:219], off
	global_load_dwordx4 v[70:73], v[214:215], off offset:768
	global_load_dwordx4 v[86:89], v[216:217], off offset:768
	global_load_dwordx4 v[74:77], v[214:215], off offset:800
	global_load_dwordx4 v[90:93], v[216:217], off offset:800
	global_load_dwordx4 v[78:81], v[214:215], off offset:832
	global_load_dwordx4 v[94:97], v[216:217], off offset:832
	global_load_dwordx4 v[82:85], v[214:215], off offset:864
	global_load_dwordx4 v[98:101], v[216:217], off offset:864
	v_add_f32_e32 v102, v102, v118
	v_mul_f32_e32 v102, 0.5, v102
	v_add_f32_e32 v103, v103, v119
	v_mul_f32_e32 v103, 0.5, v103
	v_add_f32_e32 v104, v104, v120
	v_mul_f32_e32 v104, 0.5, v104
	s_waitcnt lgkmcnt(15)
	v_mfma_f32_32x32x2_f32 a[0:15], v102, v198, a[0:15]
	v_add_f32_e32 v105, v105, v121
	v_mul_f32_e32 v105, 0.5, v105
	s_waitcnt lgkmcnt(14)
	v_mfma_f32_32x32x2_f32 a[0:15], v103, v199, a[0:15]
	v_add_f32_e32 v106, v106, v122
	v_mul_f32_e32 v106, 0.5, v106
	s_waitcnt lgkmcnt(13)
	v_mfma_f32_32x32x2_f32 a[0:15], v104, v200, a[0:15]
	v_add_f32_e32 v107, v107, v123
	v_mul_f32_e32 v107, 0.5, v107
	s_waitcnt lgkmcnt(12)
	v_mfma_f32_32x32x2_f32 a[0:15], v105, v201, a[0:15]
	v_add_f32_e32 v108, v108, v124
	v_mul_f32_e32 v108, 0.5, v108
	s_waitcnt lgkmcnt(11)
	v_mfma_f32_32x32x2_f32 a[0:15], v106, v202, a[0:15]
	v_add_f32_e32 v109, v109, v125
	v_mul_f32_e32 v109, 0.5, v109
	s_waitcnt lgkmcnt(10)
	v_mfma_f32_32x32x2_f32 a[0:15], v107, v203, a[0:15]
	v_add_f32_e32 v110, v110, v126
	v_mul_f32_e32 v110, 0.5, v110
	s_waitcnt lgkmcnt(9)
	v_mfma_f32_32x32x2_f32 a[0:15], v108, v204, a[0:15]
	v_add_f32_e32 v111, v111, v127
	v_mul_f32_e32 v111, 0.5, v111
	s_waitcnt lgkmcnt(8)
	v_mfma_f32_32x32x2_f32 a[0:15], v109, v205, a[0:15]
	v_add_f32_e32 v112, v112, v128
	v_mul_f32_e32 v112, 0.5, v112
	s_waitcnt lgkmcnt(7)
	v_mfma_f32_32x32x2_f32 a[0:15], v110, v206, a[0:15]
	v_add_f32_e32 v113, v113, v129
	v_mul_f32_e32 v113, 0.5, v113
	s_waitcnt lgkmcnt(6)
	v_mfma_f32_32x32x2_f32 a[0:15], v111, v207, a[0:15]
	v_add_f32_e32 v114, v114, v130
	v_mul_f32_e32 v114, 0.5, v114
	s_waitcnt lgkmcnt(5)
	v_mfma_f32_32x32x2_f32 a[0:15], v112, v208, a[0:15]
	v_add_f32_e32 v115, v115, v131
	v_mul_f32_e32 v115, 0.5, v115
	s_waitcnt lgkmcnt(4)
	v_mfma_f32_32x32x2_f32 a[0:15], v113, v209, a[0:15]
	v_add_f32_e32 v116, v116, v132
	v_mul_f32_e32 v116, 0.5, v116
	s_waitcnt lgkmcnt(3)
	v_mfma_f32_32x32x2_f32 a[0:15], v114, v210, a[0:15]
	v_add_f32_e32 v117, v117, v133
	v_mul_f32_e32 v117, 0.5, v117
	s_waitcnt lgkmcnt(2)
	v_mfma_f32_32x32x2_f32 a[0:15], v115, v211, a[0:15]
	s_waitcnt lgkmcnt(1)
	v_mfma_f32_32x32x2_f32 a[0:15], v116, v212, a[0:15]
	s_waitcnt lgkmcnt(0)
	v_mfma_f32_32x32x2_f32 a[0:15], v117, v213, a[0:15]
	s_waitcnt vmcnt(20)
	ds_read_b32 v198, v222 offset:0
	ds_read_b32 v199, v222 offset:128
	ds_read_b32 v200, v222 offset:256
	ds_read_b32 v201, v222 offset:384
	ds_read_b32 v202, v222 offset:1024
	ds_read_b32 v203, v222 offset:1152
	ds_read_b32 v204, v222 offset:1280
	ds_read_b32 v205, v222 offset:1408
	ds_read_b32 v206, v222 offset:2048
	ds_read_b32 v207, v222 offset:2176
	ds_read_b32 v208, v222 offset:2304
	ds_read_b32 v209, v222 offset:2432
	ds_read_b32 v210, v222 offset:3072
	ds_read_b32 v211, v222 offset:3200
	ds_read_b32 v212, v222 offset:3328
	ds_read_b32 v213, v222 offset:3456
	s_add_i32 s28, s40, 8192
	s_mov_b32 s42, 0x50000
	s_mov_b32 m0, s28
	v_lshl_add_u64 v[218:219], v[220:221], 0, s[42:43]
	global_load_lds_dwordx4 v[218:219], off
	s_add_i32 s28, s40, 9216
	s_mov_b32 s42, 0x54000
	s_mov_b32 m0, s28
	v_lshl_add_u64 v[218:219], v[220:221], 0, s[42:43]
	global_load_lds_dwordx4 v[218:219], off
	s_add_i32 s28, s40, 10240
	s_mov_b32 s42, 0x58000
	s_mov_b32 m0, s28
	v_lshl_add_u64 v[218:219], v[220:221], 0, s[42:43]
	global_load_lds_dwordx4 v[218:219], off
	s_add_i32 s28, s40, 11264
	s_mov_b32 s42, 0x5c000
	s_mov_b32 m0, s28
	v_lshl_add_u64 v[218:219], v[220:221], 0, s[42:43]
	global_load_lds_dwordx4 v[218:219], off
	global_load_dwordx4 v[102:105], v[214:215], off offset:896
	global_load_dwordx4 v[118:121], v[216:217], off offset:896
	global_load_dwordx4 v[106:109], v[214:215], off offset:928
	global_load_dwordx4 v[122:125], v[216:217], off offset:928
	global_load_dwordx4 v[110:113], v[214:215], off offset:960
	global_load_dwordx4 v[126:129], v[216:217], off offset:960
	global_load_dwordx4 v[114:117], v[214:215], off offset:992
	global_load_dwordx4 v[130:133], v[216:217], off offset:992
	v_add_f32_e32 v134, v134, v150
	v_mul_f32_e32 v134, 0.5, v134
	v_add_f32_e32 v135, v135, v151
	v_mul_f32_e32 v135, 0.5, v135
	v_add_f32_e32 v136, v136, v152
	v_mul_f32_e32 v136, 0.5, v136
	s_waitcnt lgkmcnt(15)
	v_mfma_f32_32x32x2_f32 a[0:15], v134, v198, a[0:15]
	v_add_f32_e32 v137, v137, v153
	v_mul_f32_e32 v137, 0.5, v137
	s_waitcnt lgkmcnt(14)
	v_mfma_f32_32x32x2_f32 a[0:15], v135, v199, a[0:15]
	v_add_f32_e32 v138, v138, v154
	v_mul_f32_e32 v138, 0.5, v138
	s_waitcnt lgkmcnt(13)
	v_mfma_f32_32x32x2_f32 a[0:15], v136, v200, a[0:15]
	v_add_f32_e32 v139, v139, v155
	v_mul_f32_e32 v139, 0.5, v139
	s_waitcnt lgkmcnt(12)
	v_mfma_f32_32x32x2_f32 a[0:15], v137, v201, a[0:15]
	v_add_f32_e32 v140, v140, v156
	v_mul_f32_e32 v140, 0.5, v140
	s_waitcnt lgkmcnt(11)
	v_mfma_f32_32x32x2_f32 a[0:15], v138, v202, a[0:15]
	v_add_f32_e32 v141, v141, v157
	v_mul_f32_e32 v141, 0.5, v141
	s_waitcnt lgkmcnt(10)
	v_mfma_f32_32x32x2_f32 a[0:15], v139, v203, a[0:15]
	v_add_f32_e32 v142, v142, v158
	v_mul_f32_e32 v142, 0.5, v142
	s_waitcnt lgkmcnt(9)
	v_mfma_f32_32x32x2_f32 a[0:15], v140, v204, a[0:15]
	v_add_f32_e32 v143, v143, v159
	v_mul_f32_e32 v143, 0.5, v143
	s_waitcnt lgkmcnt(8)
	v_mfma_f32_32x32x2_f32 a[0:15], v141, v205, a[0:15]
	v_add_f32_e32 v144, v144, v160
	v_mul_f32_e32 v144, 0.5, v144
	s_waitcnt lgkmcnt(7)
	v_mfma_f32_32x32x2_f32 a[0:15], v142, v206, a[0:15]
	v_add_f32_e32 v145, v145, v161
	v_mul_f32_e32 v145, 0.5, v145
	s_waitcnt lgkmcnt(6)
	v_mfma_f32_32x32x2_f32 a[0:15], v143, v207, a[0:15]
	v_add_f32_e32 v146, v146, v162
	v_mul_f32_e32 v146, 0.5, v146
	s_waitcnt lgkmcnt(5)
	v_mfma_f32_32x32x2_f32 a[0:15], v144, v208, a[0:15]
	v_add_f32_e32 v147, v147, v163
	v_mul_f32_e32 v147, 0.5, v147
	s_waitcnt lgkmcnt(4)
	v_mfma_f32_32x32x2_f32 a[0:15], v145, v209, a[0:15]
	v_add_f32_e32 v148, v148, v164
	v_mul_f32_e32 v148, 0.5, v148
	s_waitcnt lgkmcnt(3)
	v_mfma_f32_32x32x2_f32 a[0:15], v146, v210, a[0:15]
	v_add_f32_e32 v149, v149, v165
	v_mul_f32_e32 v149, 0.5, v149
	s_waitcnt lgkmcnt(2)
	v_mfma_f32_32x32x2_f32 a[0:15], v147, v211, a[0:15]
	s_waitcnt lgkmcnt(1)
	v_mfma_f32_32x32x2_f32 a[0:15], v148, v212, a[0:15]
	s_waitcnt lgkmcnt(0)
	v_mfma_f32_32x32x2_f32 a[0:15], v149, v213, a[0:15]
	s_waitcnt vmcnt(20)
	ds_read_b32 v198, v222 offset:4096
	ds_read_b32 v199, v222 offset:4224
	ds_read_b32 v200, v222 offset:4352
	ds_read_b32 v201, v222 offset:4480
	ds_read_b32 v202, v222 offset:5120
	ds_read_b32 v203, v222 offset:5248
	ds_read_b32 v204, v222 offset:5376
	ds_read_b32 v205, v222 offset:5504
	ds_read_b32 v206, v222 offset:6144
	ds_read_b32 v207, v222 offset:6272
	ds_read_b32 v208, v222 offset:6400
	ds_read_b32 v209, v222 offset:6528
	ds_read_b32 v210, v222 offset:7168
	ds_read_b32 v211, v222 offset:7296
	ds_read_b32 v212, v222 offset:7424
	ds_read_b32 v213, v222 offset:7552
	s_add_i32 s28, s40, 0
	s_mov_b32 s42, 0x60000
	s_mov_b32 m0, s28
	v_lshl_add_u64 v[218:219], v[220:221], 0, s[42:43]
	global_load_lds_dwordx4 v[218:219], off
	s_add_i32 s28, s40, 1024
	s_mov_b32 s42, 0x64000
	s_mov_b32 m0, s28
	v_lshl_add_u64 v[218:219], v[220:221], 0, s[42:43]
	global_load_lds_dwordx4 v[218:219], off
	s_add_i32 s28, s40, 2048
	s_mov_b32 s42, 0x68000
	s_mov_b32 m0, s28
	v_lshl_add_u64 v[218:219], v[220:221], 0, s[42:43]
	global_load_lds_dwordx4 v[218:219], off
	s_add_i32 s28, s40, 3072
	s_mov_b32 s42, 0x6c000
	s_mov_b32 m0, s28
	v_lshl_add_u64 v[218:219], v[220:221], 0, s[42:43]
	global_load_lds_dwordx4 v[218:219], off
	v_add_f32_e32 v166, v166, v182
	v_mul_f32_e32 v166, 0.5, v166
	v_add_f32_e32 v167, v167, v183
	v_mul_f32_e32 v167, 0.5, v167
	v_add_f32_e32 v168, v168, v184
	v_mul_f32_e32 v168, 0.5, v168
	s_waitcnt lgkmcnt(15)
	v_mfma_f32_32x32x2_f32 a[0:15], v166, v198, a[0:15]
	v_add_f32_e32 v169, v169, v185
	v_mul_f32_e32 v169, 0.5, v169
	s_waitcnt lgkmcnt(14)
	v_mfma_f32_32x32x2_f32 a[0:15], v167, v199, a[0:15]
	v_add_f32_e32 v170, v170, v186
	v_mul_f32_e32 v170, 0.5, v170
	s_waitcnt lgkmcnt(13)
	v_mfma_f32_32x32x2_f32 a[0:15], v168, v200, a[0:15]
	v_add_f32_e32 v171, v171, v187
	v_mul_f32_e32 v171, 0.5, v171
	s_waitcnt lgkmcnt(12)
	v_mfma_f32_32x32x2_f32 a[0:15], v169, v201, a[0:15]
	v_add_f32_e32 v172, v172, v188
	v_mul_f32_e32 v172, 0.5, v172
	s_waitcnt lgkmcnt(11)
	v_mfma_f32_32x32x2_f32 a[0:15], v170, v202, a[0:15]
	v_add_f32_e32 v173, v173, v189
	v_mul_f32_e32 v173, 0.5, v173
	s_waitcnt lgkmcnt(10)
	v_mfma_f32_32x32x2_f32 a[0:15], v171, v203, a[0:15]
	v_add_f32_e32 v174, v174, v190
	v_mul_f32_e32 v174, 0.5, v174
	s_waitcnt lgkmcnt(9)
	v_mfma_f32_32x32x2_f32 a[0:15], v172, v204, a[0:15]
	v_add_f32_e32 v175, v175, v191
	v_mul_f32_e32 v175, 0.5, v175
	s_waitcnt lgkmcnt(8)
	v_mfma_f32_32x32x2_f32 a[0:15], v173, v205, a[0:15]
	v_add_f32_e32 v176, v176, v192
	v_mul_f32_e32 v176, 0.5, v176
	s_waitcnt lgkmcnt(7)
	v_mfma_f32_32x32x2_f32 a[0:15], v174, v206, a[0:15]
	v_add_f32_e32 v177, v177, v193
	v_mul_f32_e32 v177, 0.5, v177
	s_waitcnt lgkmcnt(6)
	v_mfma_f32_32x32x2_f32 a[0:15], v175, v207, a[0:15]
	v_add_f32_e32 v178, v178, v194
	v_mul_f32_e32 v178, 0.5, v178
	s_waitcnt lgkmcnt(5)
	v_mfma_f32_32x32x2_f32 a[0:15], v176, v208, a[0:15]
	v_add_f32_e32 v179, v179, v195
	v_mul_f32_e32 v179, 0.5, v179
	s_waitcnt lgkmcnt(4)
	v_mfma_f32_32x32x2_f32 a[0:15], v177, v209, a[0:15]
	v_add_f32_e32 v180, v180, v196
	v_mul_f32_e32 v180, 0.5, v180
	s_waitcnt lgkmcnt(3)
	v_mfma_f32_32x32x2_f32 a[0:15], v178, v210, a[0:15]
	v_add_f32_e32 v181, v181, v197
	v_mul_f32_e32 v181, 0.5, v181
	s_waitcnt lgkmcnt(2)
	v_mfma_f32_32x32x2_f32 a[0:15], v179, v211, a[0:15]
	s_waitcnt lgkmcnt(1)
	v_mfma_f32_32x32x2_f32 a[0:15], v180, v212, a[0:15]
	s_waitcnt lgkmcnt(0)
	v_mfma_f32_32x32x2_f32 a[0:15], v181, v213, a[0:15]
	s_waitcnt vmcnt(12)
	ds_read_b32 v198, v222 offset:8192
	ds_read_b32 v199, v222 offset:8320
	ds_read_b32 v200, v222 offset:8448
	ds_read_b32 v201, v222 offset:8576
	ds_read_b32 v202, v222 offset:9216
	ds_read_b32 v203, v222 offset:9344
	ds_read_b32 v204, v222 offset:9472
	ds_read_b32 v205, v222 offset:9600
	ds_read_b32 v206, v222 offset:10240
	ds_read_b32 v207, v222 offset:10368
	ds_read_b32 v208, v222 offset:10496
	ds_read_b32 v209, v222 offset:10624
	ds_read_b32 v210, v222 offset:11264
	ds_read_b32 v211, v222 offset:11392
	ds_read_b32 v212, v222 offset:11520
	ds_read_b32 v213, v222 offset:11648
	s_add_i32 s28, s40, 4096
	s_mov_b32 s42, 0x70000
	s_mov_b32 m0, s28
	v_lshl_add_u64 v[218:219], v[220:221], 0, s[42:43]
	global_load_lds_dwordx4 v[218:219], off
	s_add_i32 s28, s40, 5120
	s_mov_b32 s42, 0x74000
	s_mov_b32 m0, s28
	v_lshl_add_u64 v[218:219], v[220:221], 0, s[42:43]
	global_load_lds_dwordx4 v[218:219], off
	s_add_i32 s28, s40, 6144
	s_mov_b32 s42, 0x78000
	s_mov_b32 m0, s28
	v_lshl_add_u64 v[218:219], v[220:221], 0, s[42:43]
	global_load_lds_dwordx4 v[218:219], off
	s_add_i32 s28, s40, 7168
	s_mov_b32 s42, 0x7c000
	s_mov_b32 m0, s28
	v_lshl_add_u64 v[218:219], v[220:221], 0, s[42:43]
	global_load_lds_dwordx4 v[218:219], off
	v_add_f32_e32 v38, v38, v54
	v_mul_f32_e32 v38, 0.5, v38
	v_add_f32_e32 v39, v39, v55
	v_mul_f32_e32 v39, 0.5, v39
	v_add_f32_e32 v40, v40, v56
	v_mul_f32_e32 v40, 0.5, v40
	s_waitcnt lgkmcnt(15)
	v_mfma_f32_32x32x2_f32 a[0:15], v38, v198, a[0:15]
	v_add_f32_e32 v41, v41, v57
	v_mul_f32_e32 v41, 0.5, v41
	s_waitcnt lgkmcnt(14)
	v_mfma_f32_32x32x2_f32 a[0:15], v39, v199, a[0:15]
	v_add_f32_e32 v42, v42, v58
	v_mul_f32_e32 v42, 0.5, v42
	s_waitcnt lgkmcnt(13)
	v_mfma_f32_32x32x2_f32 a[0:15], v40, v200, a[0:15]
	v_add_f32_e32 v43, v43, v59
	v_mul_f32_e32 v43, 0.5, v43
	s_waitcnt lgkmcnt(12)
	v_mfma_f32_32x32x2_f32 a[0:15], v41, v201, a[0:15]
	v_add_f32_e32 v44, v44, v60
	v_mul_f32_e32 v44, 0.5, v44
	s_waitcnt lgkmcnt(11)
	v_mfma_f32_32x32x2_f32 a[0:15], v42, v202, a[0:15]
	v_add_f32_e32 v45, v45, v61
	v_mul_f32_e32 v45, 0.5, v45
	s_waitcnt lgkmcnt(10)
	v_mfma_f32_32x32x2_f32 a[0:15], v43, v203, a[0:15]
	v_add_f32_e32 v46, v46, v62
	v_mul_f32_e32 v46, 0.5, v46
	s_waitcnt lgkmcnt(9)
	v_mfma_f32_32x32x2_f32 a[0:15], v44, v204, a[0:15]
	v_add_f32_e32 v47, v47, v63
	v_mul_f32_e32 v47, 0.5, v47
	s_waitcnt lgkmcnt(8)
	v_mfma_f32_32x32x2_f32 a[0:15], v45, v205, a[0:15]
	v_add_f32_e32 v48, v48, v64
	v_mul_f32_e32 v48, 0.5, v48
	s_waitcnt lgkmcnt(7)
	v_mfma_f32_32x32x2_f32 a[0:15], v46, v206, a[0:15]
	v_add_f32_e32 v49, v49, v65
	v_mul_f32_e32 v49, 0.5, v49
	s_waitcnt lgkmcnt(6)
	v_mfma_f32_32x32x2_f32 a[0:15], v47, v207, a[0:15]
	v_add_f32_e32 v50, v50, v66
	v_mul_f32_e32 v50, 0.5, v50
	s_waitcnt lgkmcnt(5)
	v_mfma_f32_32x32x2_f32 a[0:15], v48, v208, a[0:15]
	v_add_f32_e32 v51, v51, v67
	v_mul_f32_e32 v51, 0.5, v51
	s_waitcnt lgkmcnt(4)
	v_mfma_f32_32x32x2_f32 a[0:15], v49, v209, a[0:15]
	v_add_f32_e32 v52, v52, v68
	v_mul_f32_e32 v52, 0.5, v52
	s_waitcnt lgkmcnt(3)
	v_mfma_f32_32x32x2_f32 a[0:15], v50, v210, a[0:15]
	v_add_f32_e32 v53, v53, v69
	v_mul_f32_e32 v53, 0.5, v53
	s_waitcnt lgkmcnt(2)
	v_mfma_f32_32x32x2_f32 a[0:15], v51, v211, a[0:15]
	s_waitcnt lgkmcnt(1)
	v_mfma_f32_32x32x2_f32 a[0:15], v52, v212, a[0:15]
	s_waitcnt lgkmcnt(0)
	v_mfma_f32_32x32x2_f32 a[0:15], v53, v213, a[0:15]
	s_waitcnt vmcnt(4)
	ds_read_b32 v198, v222 offset:0
	ds_read_b32 v199, v222 offset:128
	ds_read_b32 v200, v222 offset:256
	ds_read_b32 v201, v222 offset:384
	ds_read_b32 v202, v222 offset:1024
	ds_read_b32 v203, v222 offset:1152
	ds_read_b32 v204, v222 offset:1280
	ds_read_b32 v205, v222 offset:1408
	ds_read_b32 v206, v222 offset:2048
	ds_read_b32 v207, v222 offset:2176
	ds_read_b32 v208, v222 offset:2304
	ds_read_b32 v209, v222 offset:2432
	ds_read_b32 v210, v222 offset:3072
	ds_read_b32 v211, v222 offset:3200
	ds_read_b32 v212, v222 offset:3328
	ds_read_b32 v213, v222 offset:3456
	v_add_f32_e32 v70, v70, v86
	v_mul_f32_e32 v70, 0.5, v70
	v_add_f32_e32 v71, v71, v87
	v_mul_f32_e32 v71, 0.5, v71
	v_add_f32_e32 v72, v72, v88
	v_mul_f32_e32 v72, 0.5, v72
	s_waitcnt lgkmcnt(15)
	v_mfma_f32_32x32x2_f32 a[0:15], v70, v198, a[0:15]
	v_add_f32_e32 v73, v73, v89
	v_mul_f32_e32 v73, 0.5, v73
	s_waitcnt lgkmcnt(14)
	v_mfma_f32_32x32x2_f32 a[0:15], v71, v199, a[0:15]
	v_add_f32_e32 v74, v74, v90
	v_mul_f32_e32 v74, 0.5, v74
	s_waitcnt lgkmcnt(13)
	v_mfma_f32_32x32x2_f32 a[0:15], v72, v200, a[0:15]
	v_add_f32_e32 v75, v75, v91
	v_mul_f32_e32 v75, 0.5, v75
	s_waitcnt lgkmcnt(12)
	v_mfma_f32_32x32x2_f32 a[0:15], v73, v201, a[0:15]
	v_add_f32_e32 v76, v76, v92
	v_mul_f32_e32 v76, 0.5, v76
	s_waitcnt lgkmcnt(11)
	v_mfma_f32_32x32x2_f32 a[0:15], v74, v202, a[0:15]
	v_add_f32_e32 v77, v77, v93
	v_mul_f32_e32 v77, 0.5, v77
	s_waitcnt lgkmcnt(10)
	v_mfma_f32_32x32x2_f32 a[0:15], v75, v203, a[0:15]
	v_add_f32_e32 v78, v78, v94
	v_mul_f32_e32 v78, 0.5, v78
	s_waitcnt lgkmcnt(9)
	v_mfma_f32_32x32x2_f32 a[0:15], v76, v204, a[0:15]
	v_add_f32_e32 v79, v79, v95
	v_mul_f32_e32 v79, 0.5, v79
	s_waitcnt lgkmcnt(8)
	v_mfma_f32_32x32x2_f32 a[0:15], v77, v205, a[0:15]
	v_add_f32_e32 v80, v80, v96
	v_mul_f32_e32 v80, 0.5, v80
	s_waitcnt lgkmcnt(7)
	v_mfma_f32_32x32x2_f32 a[0:15], v78, v206, a[0:15]
	v_add_f32_e32 v81, v81, v97
	v_mul_f32_e32 v81, 0.5, v81
	s_waitcnt lgkmcnt(6)
	v_mfma_f32_32x32x2_f32 a[0:15], v79, v207, a[0:15]
	v_add_f32_e32 v82, v82, v98
	v_mul_f32_e32 v82, 0.5, v82
	s_waitcnt lgkmcnt(5)
	v_mfma_f32_32x32x2_f32 a[0:15], v80, v208, a[0:15]
	v_add_f32_e32 v83, v83, v99
	v_mul_f32_e32 v83, 0.5, v83
	s_waitcnt lgkmcnt(4)
	v_mfma_f32_32x32x2_f32 a[0:15], v81, v209, a[0:15]
	v_add_f32_e32 v84, v84, v100
	v_mul_f32_e32 v84, 0.5, v84
	s_waitcnt lgkmcnt(3)
	v_mfma_f32_32x32x2_f32 a[0:15], v82, v210, a[0:15]
	v_add_f32_e32 v85, v85, v101
	v_mul_f32_e32 v85, 0.5, v85
	s_waitcnt lgkmcnt(2)
	v_mfma_f32_32x32x2_f32 a[0:15], v83, v211, a[0:15]
	s_waitcnt lgkmcnt(1)
	v_mfma_f32_32x32x2_f32 a[0:15], v84, v212, a[0:15]
	s_waitcnt lgkmcnt(0)
	v_mfma_f32_32x32x2_f32 a[0:15], v85, v213, a[0:15]
	s_waitcnt vmcnt(0)
	ds_read_b32 v198, v222 offset:4096
	ds_read_b32 v199, v222 offset:4224
	ds_read_b32 v200, v222 offset:4352
	ds_read_b32 v201, v222 offset:4480
	ds_read_b32 v202, v222 offset:5120
	ds_read_b32 v203, v222 offset:5248
	ds_read_b32 v204, v222 offset:5376
	ds_read_b32 v205, v222 offset:5504
	ds_read_b32 v206, v222 offset:6144
	ds_read_b32 v207, v222 offset:6272
	ds_read_b32 v208, v222 offset:6400
	ds_read_b32 v209, v222 offset:6528
	ds_read_b32 v210, v222 offset:7168
	ds_read_b32 v211, v222 offset:7296
	ds_read_b32 v212, v222 offset:7424
	ds_read_b32 v213, v222 offset:7552
	v_add_f32_e32 v102, v102, v118
	v_mul_f32_e32 v102, 0.5, v102
	v_add_f32_e32 v103, v103, v119
	v_mul_f32_e32 v103, 0.5, v103
	v_add_f32_e32 v104, v104, v120
	v_mul_f32_e32 v104, 0.5, v104
	s_waitcnt lgkmcnt(15)
	v_mfma_f32_32x32x2_f32 a[0:15], v102, v198, a[0:15]
	v_add_f32_e32 v105, v105, v121
	v_mul_f32_e32 v105, 0.5, v105
	s_waitcnt lgkmcnt(14)
	v_mfma_f32_32x32x2_f32 a[0:15], v103, v199, a[0:15]
	v_add_f32_e32 v106, v106, v122
	v_mul_f32_e32 v106, 0.5, v106
	s_waitcnt lgkmcnt(13)
	v_mfma_f32_32x32x2_f32 a[0:15], v104, v200, a[0:15]
	v_add_f32_e32 v107, v107, v123
	v_mul_f32_e32 v107, 0.5, v107
	s_waitcnt lgkmcnt(12)
	v_mfma_f32_32x32x2_f32 a[0:15], v105, v201, a[0:15]
	v_add_f32_e32 v108, v108, v124
	v_mul_f32_e32 v108, 0.5, v108
	s_waitcnt lgkmcnt(11)
	v_mfma_f32_32x32x2_f32 a[0:15], v106, v202, a[0:15]
	v_add_f32_e32 v109, v109, v125
	v_mul_f32_e32 v109, 0.5, v109
	s_waitcnt lgkmcnt(10)
	v_mfma_f32_32x32x2_f32 a[0:15], v107, v203, a[0:15]
	v_add_f32_e32 v110, v110, v126
	v_mul_f32_e32 v110, 0.5, v110
	s_waitcnt lgkmcnt(9)
	v_mfma_f32_32x32x2_f32 a[0:15], v108, v204, a[0:15]
	v_add_f32_e32 v111, v111, v127
	v_mul_f32_e32 v111, 0.5, v111
	s_waitcnt lgkmcnt(8)
	v_mfma_f32_32x32x2_f32 a[0:15], v109, v205, a[0:15]
	v_add_f32_e32 v112, v112, v128
	v_mul_f32_e32 v112, 0.5, v112
	s_waitcnt lgkmcnt(7)
	v_mfma_f32_32x32x2_f32 a[0:15], v110, v206, a[0:15]
	v_add_f32_e32 v113, v113, v129
	v_mul_f32_e32 v113, 0.5, v113
	s_waitcnt lgkmcnt(6)
	v_mfma_f32_32x32x2_f32 a[0:15], v111, v207, a[0:15]
	v_add_f32_e32 v114, v114, v130
	v_mul_f32_e32 v114, 0.5, v114
	s_waitcnt lgkmcnt(5)
	v_mfma_f32_32x32x2_f32 a[0:15], v112, v208, a[0:15]
	v_add_f32_e32 v115, v115, v131
	v_mul_f32_e32 v115, 0.5, v115
	s_waitcnt lgkmcnt(4)
	v_mfma_f32_32x32x2_f32 a[0:15], v113, v209, a[0:15]
	v_add_f32_e32 v116, v116, v132
	v_mul_f32_e32 v116, 0.5, v116
	s_waitcnt lgkmcnt(3)
	v_mfma_f32_32x32x2_f32 a[0:15], v114, v210, a[0:15]
	v_add_f32_e32 v117, v117, v133
	v_mul_f32_e32 v117, 0.5, v117
	s_waitcnt lgkmcnt(2)
	v_mfma_f32_32x32x2_f32 a[0:15], v115, v211, a[0:15]
	s_waitcnt lgkmcnt(1)
	v_mfma_f32_32x32x2_f32 a[0:15], v116, v212, a[0:15]
	s_waitcnt lgkmcnt(0)
	v_mfma_f32_32x32x2_f32 a[0:15], v117, v213, a[0:15]
	s_mov_b32 s30, 0x80000
	s_mov_b32 s31, 0
	s_nop 1
	s_lshl_b32 s28, s34, 5
	s_and_b32 s28, s28, 0x1e0
	v_or_b32_e32 v14, s28, v2
	v_lshlrev_b32_e32 v14, 2, v14
	s_nop 12
	ds_write_b32 v3, a0
	ds_write_b32 v3, a1 offset:256
	ds_write_b32 v3, a2 offset:512
	ds_write_b32 v3, a3 offset:768
	ds_write_b32 v3, a4 offset:1024
	ds_write_b32 v3, a5 offset:1280
	ds_write_b32 v3, a6 offset:1536
	ds_write_b32 v3, a7 offset:1792
	ds_write_b32 v3, a8 offset:2048
	ds_write_b32 v3, a9 offset:2304
	ds_write_b32 v3, a10 offset:2560
	ds_write_b32 v3, a11 offset:2816
	ds_write_b32 v3, a12 offset:3072
	ds_write_b32 v3, a13 offset:3328
	ds_write_b32 v3, a14 offset:3584
	ds_write_b32 v3, a15 offset:3840
	s_waitcnt lgkmcnt(0)
	s_barrier
	global_load_dword v37, v14, s[22:23]
	global_load_dword v42, v14, s[26:27]
	ds_read2st64_b32 v[14:15], v28 offset1:4
	ds_read2st64_b32 v[16:17], v28 offset0:16 offset1:20
	ds_read2st64_b32 v[18:19], v28 offset0:32 offset1:36
	ds_read2st64_b32 v[20:21], v28 offset0:48 offset1:52
	ds_read2st64_b32 v[22:23], v28 offset0:8 offset1:12
	ds_read2st64_b32 v[24:25], v28 offset0:24 offset1:28
	ds_read2st64_b32 v[38:39], v28 offset0:40 offset1:44
	ds_read2st64_b32 v[40:41], v28 offset0:56 offset1:60
	s_waitcnt lgkmcnt(6)
	v_add_f32_e32 v14, v14, v16
	v_add_f32_e32 v15, v15, v17
	s_waitcnt lgkmcnt(5)
	v_add_f32_e32 v14, v14, v18
	s_waitcnt lgkmcnt(2)
	v_add_f32_e32 v16, v22, v24
	v_add_f32_e32 v15, v15, v19
	v_add_f32_e32 v14, v14, v20
	v_add_f32_e32 v17, v23, v25
	s_waitcnt lgkmcnt(1)
	v_add_f32_e32 v16, v16, v38
	v_add_f32_e32 v15, v15, v21
	v_add_f32_e32 v17, v17, v39
	s_waitcnt lgkmcnt(0)
	v_add_f32_e32 v16, v16, v40
	v_add_f32_e32 v17, v17, v41
	v_cmp_lt_i32_e32 vcc, v31, v30
	s_waitcnt vmcnt(1)
	v_add_f32_e32 v14, v14, v37
	v_add_f32_e32 v15, v15, v37
	v_max_f32_e32 v14, 0, v14
	v_add_f32_e32 v16, v16, v37
	v_max_f32_e32 v15, 0, v15
	s_waitcnt vmcnt(0)
	v_fma_f32 v14, v42, v14, 0
	v_add_f32_e32 v17, v17, v37
	v_max_f32_e32 v16, 0, v16
	v_fmac_f32_e32 v14, v42, v15
	v_cndmask_b32_e32 v43, v29, v31, vcc
	v_max_f32_e32 v17, 0, v17
	v_fmac_f32_e32 v14, v42, v16
	v_lshlrev_b32_e32 v43, 2, v43
	v_fmac_f32_e32 v14, v42, v17
	ds_bpermute_b32 v15, v43, v14
	v_cmp_lt_i32_e32 vcc, v32, v30
	s_waitcnt lgkmcnt(0)
	v_add_f32_e32 v14, v14, v15
	v_cndmask_b32_e32 v16, v29, v32, vcc
	v_lshlrev_b32_e32 v16, 2, v16
	ds_bpermute_b32 v15, v16, v14
	v_cmp_lt_i32_e32 vcc, v33, v30
	s_waitcnt lgkmcnt(0)
	v_add_f32_e32 v14, v14, v15
	v_cndmask_b32_e32 v16, v29, v33, vcc
	v_lshlrev_b32_e32 v16, 2, v16
	ds_bpermute_b32 v15, v16, v14
	v_cmp_lt_i32_e32 vcc, v34, v30
	s_waitcnt lgkmcnt(0)
	v_add_f32_e32 v14, v14, v15
	v_cndmask_b32_e32 v16, v29, v34, vcc
	v_lshlrev_b32_e32 v16, 2, v16
	ds_bpermute_b32 v15, v16, v14
	v_cmp_lt_i32_e32 vcc, v35, v30
	s_waitcnt lgkmcnt(0)
	v_add_f32_e32 v14, v14, v15
	v_cndmask_b32_e32 v16, v29, v35, vcc
	v_lshlrev_b32_e32 v16, 2, v16
	ds_bpermute_b32 v15, v16, v14
	v_cmp_lt_i32_e32 vcc, v36, v30
	s_waitcnt lgkmcnt(0)
	v_add_f32_e32 v14, v14, v15
	v_cndmask_b32_e32 v16, v29, v36, vcc
	v_lshlrev_b32_e32 v15, 2, v16
	ds_bpermute_b32 v15, v15, v14
	s_and_saveexec_b64 s[30:31], s[8:9]
	s_cbranch_execz .LBB2_18
	s_waitcnt lgkmcnt(0)
	v_add_f32_e32 v14, v14, v15
	ds_write_b32 v27, v14

	.amdhsa_kernel _Z20refine_gather_kernelPKfS0_S0_S0_S0_S0_S0_PfPiS1_
		.amdhsa_group_segment_fixed_size 65600
		.amdhsa_private_segment_fixed_size 0
		.amdhsa_kernarg_size 80
		.amdhsa_user_sgpr_count 2
		.amdhsa_user_sgpr_dispatch_ptr 0
		.amdhsa_user_sgpr_queue_ptr 0
		.amdhsa_user_sgpr_kernarg_segment_ptr 1
		.amdhsa_user_sgpr_dispatch_id 0
		.amdhsa_user_sgpr_kernarg_preload_length 0
		.amdhsa_user_sgpr_kernarg_preload_offset 0
		.amdhsa_user_sgpr_private_segment_size 0
		.amdhsa_uses_dynamic_stack 0
		.amdhsa_enable_private_segment 0
		.amdhsa_system_sgpr_workgroup_id_x 1
		.amdhsa_system_sgpr_workgroup_id_y 0
		.amdhsa_system_sgpr_workgroup_id_z 0
		.amdhsa_system_sgpr_workgroup_info 0
		.amdhsa_system_vgpr_workitem_id 0
		.amdhsa_next_free_vgpr 256
		.amdhsa_next_free_sgpr 100
		.amdhsa_accum_offset 240
		.amdhsa_reserve_vcc 1
		.amdhsa_float_round_mode_32 0
		.amdhsa_float_round_mode_16_64 0
		.amdhsa_float_denorm_mode_32 3
		.amdhsa_float_denorm_mode_16_64 3
		.amdhsa_dx10_clamp 1
		.amdhsa_ieee_mode 1
		.amdhsa_fp16_overflow 0
		.amdhsa_tg_split 0
		.amdhsa_exception_fp_ieee_invalid_op 0
		.amdhsa_exception_fp_denorm_src 0
		.amdhsa_exception_fp_ieee_div_zero 0
		.amdhsa_exception_fp_ieee_overflow 0
		.amdhsa_exception_fp_ieee_underflow 0
		.amdhsa_exception_fp_ieee_inexact 0
		.amdhsa_exception_int_div_zero 0
	.end_amdhsa_kernel

amdhsa.kernels:
  - .agpr_count:     0
    .args:
      - .actual_access:  read_only
        .address_space:  global
        .offset:         0
        .size:           8
        .value_kind:     global_buffer
      - .actual_access:  write_only
        .address_space:  global
        .offset:         8
        .size:           8
        .value_kind:     global_buffer
    .group_segment_fixed_size: 0
    .kernarg_segment_align: 8
    .kernarg_segment_size: 16
    .language:       OpenCL C
    .language_version:
      - 2
      - 0
    .max_flat_workgroup_size: 256
    .name:           _Z7prep_w1PKfPDv8_DF16_
    .private_segment_fixed_size: 0
    .sgpr_count:     14
    .sgpr_spill_count: 0
    .symbol:         _Z7prep_w1PKfPDv8_DF16_.kd
    .uniform_work_group_size: 1
    .uses_dynamic_stack: false
    .vgpr_count:     26
    .vgpr_spill_count: 0
    .wavefront_size: 64
  - .agpr_count:     0
    .args:
      - .address_space:  global
        .offset:         0
        .size:           8
        .value_kind:     global_buffer
      - .address_space:  global
        .offset:         8
        .size:           8
        .value_kind:     global_buffer
      - .address_space:  global
        .offset:         16
        .size:           8
        .value_kind:     global_buffer
      - .actual_access:  read_only
        .address_space:  global
        .offset:         24
        .size:           8
        .value_kind:     global_buffer
      - .actual_access:  read_only
        .address_space:  global
        .offset:         32
        .size:           8
        .value_kind:     global_buffer
      - .actual_access:  write_only
        .address_space:  global
        .offset:         40
        .size:           8
        .value_kind:     global_buffer
      - .actual_access:  write_only
        .address_space:  global
        .offset:         48
        .size:           8
        .value_kind:     global_buffer
    .group_segment_fixed_size: 163840
    .kernarg_segment_align: 8
    .kernarg_segment_size: 56
    .language:       OpenCL C
    .language_version:
      - 2
      - 0
    .max_flat_workgroup_size: 768
    .name:           _Z12score_kernelPKfS0_PKcS0_S0_PfPi
    .private_segment_fixed_size: 0
    .sgpr_count:     34
    .sgpr_spill_count: 0
    .symbol:         _Z12score_kernelPKfS0_PKcS0_S0_PfPi.kd
    .uniform_work_group_size: 1
    .uses_dynamic_stack: false
    .vgpr_count:     164
    .vgpr_spill_count: 0
    .wavefront_size: 64
  - .agpr_count:     16
    .args:
      - .actual_access:  read_only
        .address_space:  global
        .offset:         0
        .size:           8
        .value_kind:     global_buffer
      - .actual_access:  read_only
        .address_space:  global
        .offset:         8
        .size:           8
        .value_kind:     global_buffer
      - .actual_access:  read_only
        .address_space:  global
        .offset:         16
        .size:           8
        .value_kind:     global_buffer
      - .actual_access:  read_only
        .address_space:  global
        .offset:         24
        .size:           8
        .value_kind:     global_buffer
      - .actual_access:  read_only
        .address_space:  global
        .offset:         32
        .size:           8
        .value_kind:     global_buffer
      - .actual_access:  read_only
        .address_space:  global
        .offset:         40
        .size:           8
        .value_kind:     global_buffer
      - .actual_access:  read_only
        .address_space:  global
        .offset:         48
        .size:           8
        .value_kind:     global_buffer
      - .address_space:  global
        .offset:         56
        .size:           8
        .value_kind:     global_buffer
      - .address_space:  global
        .offset:         64
        .size:           8
        .value_kind:     global_buffer
      - .actual_access:  write_only
        .address_space:  global
        .offset:         72
        .size:           8
        .value_kind:     global_buffer
    .group_segment_fixed_size: 65600
    .kernarg_segment_align: 8
    .kernarg_segment_size: 80
    .language:       OpenCL C
    .language_version:
      - 2
      - 0
    .max_flat_workgroup_size: 256
    .name:           _Z20refine_gather_kernelPKfS0_S0_S0_S0_S0_S0_PfPiS1_
    .private_segment_fixed_size: 0
    .sgpr_count:     106
    .sgpr_spill_count: 94
    .symbol:         _Z20refine_gather_kernelPKfS0_S0_S0_S0_S0_S0_PfPiS1_.kd
    .uniform_work_group_size: 1
    .uses_dynamic_stack: false
    .vgpr_count:     256
    .vgpr_spill_count: 0
    .wavefront_size: 64
